# xnorm logit epilogue: lane (fr, fq) evaluates row fq of the pass (every lane already holds all four rows of its column), one trip through the gate branches instead of four serial ones on 16 lanes
# baseline (speedup 1.0000x reference)
; DI void phase_xnorm(const Params& p, int bid, int nb, char* lds) {
;     ...
;   for (int row0 = gw * 4; row0 < T_; row0 += nw * 4) {
;     const int b = row0 >> 13;
;     f32x4 v[4][4];
; #pragma unroll
;     for (int r = 0; r < 4; ++r)
; #pragma unroll
;       for (int i = 0; i < 4; ++i) v[r][i] = ((const f32x4*)(p.x + (size_t)(row0 + r) * 1024))[lane + 64 * i];
;     f32x4 g4[4], sh[4], sc[4];
; #pragma unroll
;     for (int i = 0; i < 4; ++i) { const int col = 4 * lane + 256 * i; g4[i] = *(const f32x4*)(p.g_pre_mix + col); sh[i] = *(const f32x4*)(mod + b * 6144 + col); sc[i] = *(const f32x4*)(mod + b * 6144 + 1024 + col); }
; #pragma unroll
;     for (int r = 0; r < 4; ++r) {
;       float ss = 0.f;
; #pragma unroll
;       for (int i = 0; i < 4; ++i) ss += v[r][i][0] * v[r][i][0] + v[r][i][1] * v[r][i][1] + v[r][i][2] * v[r][i][2] + v[r][i][3] * v[r][i][3];
;       ss = wave_sum(ss);
;       const float rstd = rsqrtf(ss * (1.f / 1024.f) + 1e-6f);
.LBB0_94:
	v_add_co_u32_e32 v0, vcc, 0xffffd000, v106
	v_ashrrev_i32_e32 v4, 13, v88
	s_nop 0
	v_addc_co_u32_e32 v1, vcc, -1, v107, vcc
	global_load_dwordx4 v[60:63], v[0:1], off offset:-3072
	global_load_dwordx4 v[56:59], v[0:1], off offset:-2048
	global_load_dwordx4 v[36:39], v[0:1], off offset:-1024
	global_load_dwordx4 v[32:35], v[0:1], off
	v_add_co_u32_e32 v0, vcc, 0xffffe000, v106
	v_mul_i32_i24_e32 v4, 0x1800, v4
	s_nop 0
	v_addc_co_u32_e32 v1, vcc, -1, v107, vcc
	global_load_dwordx4 v[52:55], v[0:1], off offset:-3072
	global_load_dwordx4 v[48:51], v[0:1], off offset:-2048
	global_load_dwordx4 v[44:47], v[0:1], off offset:-1024
	global_load_dwordx4 v[40:43], v[0:1], off
	v_ashrrev_i32_e32 v5, 31, v4
	v_lshl_add_u64 v[4:5], v[4:5], 2, s[20:21]
	v_lshl_add_u64 v[8:9], v[4:5], 0, s[24:25]
	v_mov_b32_e32 v109, v93
	v_mov_b32_e32 v111, v93
	v_mov_b32_e32 v113, v93
	v_lshl_add_u64 v[20:21], v[4:5], 0, v[92:93]
	v_lshl_add_u64 v[10:11], v[8:9], 0, v[92:93]
	global_load_dwordx4 v[0:3], v[94:95], off
	global_load_dwordx4 v[4:7], v[20:21], off
	v_lshl_add_u64 v[12:13], v[8:9], 0, v[108:109]
	v_lshl_add_u64 v[14:15], v[8:9], 0, v[110:111]
	v_lshl_add_u64 v[8:9], v[8:9], 0, v[112:113]
	global_load_dwordx4 v[72:75], v[10:11], off
	global_load_dwordx4 v[76:79], v[12:13], off
	global_load_dwordx4 v[68:71], v[14:15], off
	global_load_dwordx4 v[64:67], v[8:9], off
	v_add_co_u32_e32 v152, vcc, 0xfffff000, v106
	v_mov_b64_e32 v[126:127], s[28:29]
	s_nop 0
	v_addc_co_u32_e32 v153, vcc, -1, v107, vcc
	v_lshl_add_u64 v[134:135], s[84:85], 0, v[104:105]
	s_waitcnt vmcnt(13)
	v_mov_b32_e32 v10, v61
	s_waitcnt vmcnt(12)
	v_mov_b32_e32 v11, v57
	s_waitcnt vmcnt(11)
	v_mov_b32_e32 v18, v37
	s_waitcnt vmcnt(10)
	v_mov_b32_e32 v19, v33
	v_mov_b32_e32 v8, v60
	v_mov_b32_e32 v9, v56
	v_mov_b32_e32 v16, v36
	v_mov_b32_e32 v17, v32
	v_pk_mul_f32 v[10:11], v[10:11], v[10:11]
	v_pk_mul_f32 v[18:19], v[18:19], v[18:19]
	s_waitcnt vmcnt(9)
	v_mov_b32_e32 v28, v53
	s_waitcnt vmcnt(8)
	v_mov_b32_e32 v29, v49
	v_mov_b32_e32 v12, v62
	v_mov_b32_e32 v13, v58
	v_mov_b32_e32 v26, v52
	v_mov_b32_e32 v27, v48
	s_waitcnt vmcnt(7)
	v_mov_b32_e32 v84, v45
	s_waitcnt vmcnt(6)
	v_mov_b32_e32 v85, v41
	v_pk_fma_f32 v[8:9], v[8:9], v[8:9], v[10:11]
	v_pk_fma_f32 v[10:11], v[16:17], v[16:17], v[18:19]
	v_pk_mul_f32 v[16:17], v[28:29], v[28:29]
	v_mov_b32_e32 v30, v54
	v_mov_b32_e32 v31, v50
	v_mov_b32_e32 v82, v44
	v_mov_b32_e32 v83, v40
	v_pk_mul_f32 v[18:19], v[84:85], v[84:85]
	v_pk_fma_f32 v[8:9], v[12:13], v[12:13], v[8:9]
	v_pk_fma_f32 v[12:13], v[26:27], v[26:27], v[16:17]
	v_mov_b32_e32 v14, v63
	v_mov_b32_e32 v15, v59
	v_mov_b32_e32 v22, v38
	v_mov_b32_e32 v23, v34
	v_mov_b32_e32 v80, v55
	v_mov_b32_e32 v81, v51
	v_mov_b32_e32 v86, v46
	v_mov_b32_e32 v87, v42
	v_pk_fma_f32 v[16:17], v[82:83], v[82:83], v[18:19]
	v_pk_fma_f32 v[12:13], v[30:31], v[30:31], v[12:13]
	v_mov_b32_e32 v24, v39
	v_mov_b32_e32 v25, v35
	v_mov_b32_e32 v116, v47
	v_mov_b32_e32 v117, v43
	v_pk_fma_f32 v[10:11], v[22:23], v[22:23], v[10:11]
	v_pk_fma_f32 v[8:9], v[14:15], v[14:15], v[8:9]
	v_pk_fma_f32 v[14:15], v[86:87], v[86:87], v[16:17]
	v_pk_fma_f32 v[12:13], v[80:81], v[80:81], v[12:13]
	v_pk_fma_f32 v[10:11], v[24:25], v[24:25], v[10:11]
	v_pk_fma_f32 v[14:15], v[116:117], v[116:117], v[14:15]
	v_mov_b32_e32 v17, v8
	v_mov_b32_e32 v16, v12
	v_mov_b32_e32 v8, v13
	v_mov_b32_e32 v12, v14
	v_pk_add_f32 v[8:9], v[16:17], v[8:9]
	v_mov_b32_e32 v13, v10
	v_pk_add_f32 v[8:9], v[8:9], v[12:13]
	v_mov_b32_e32 v10, v15
	v_pk_add_f32 v[8:9], v[8:9], v[10:11]
	ds_bpermute_b32 v11, v91, v9
	ds_bpermute_b32 v10, v91, v8
	s_waitcnt vmcnt(3)
	v_pk_add_f32 v[122:123], v[74:75], 1.0 op_sel_hi:[1,0]
	s_waitcnt vmcnt(1)
	v_pk_add_f32 v[116:117], v[70:71], 1.0 op_sel_hi:[1,0]
	v_pk_add_f32 v[124:125], v[72:73], 1.0 op_sel_hi:[1,0]
	v_pk_add_f32 v[118:119], v[78:79], 1.0 op_sel_hi:[1,0]
	s_waitcnt lgkmcnt(0)
	v_pk_add_f32 v[8:9], v[8:9], v[10:11]
	ds_bpermute_b32 v11, v136, v9
	ds_bpermute_b32 v10, v136, v8
	v_pk_add_f32 v[120:121], v[76:77], 1.0 op_sel_hi:[1,0]
	s_waitcnt vmcnt(0)
	v_pk_add_f32 v[130:131], v[64:65], 1.0 op_sel_hi:[1,0]
	v_pk_add_f32 v[132:133], v[68:69], 1.0 op_sel_hi:[1,0]
	v_pk_add_f32 v[128:129], v[66:67], 1.0 op_sel_hi:[1,0]
	s_waitcnt lgkmcnt(0)
	v_pk_add_f32 v[22:23], v[8:9], v[10:11]
	ds_bpermute_b32 v25, v137, v23
	ds_bpermute_b32 v24, v137, v22
	global_load_dwordx4 v[16:19], v[94:95], off offset:1024
	global_load_dwordx4 v[12:15], v[94:95], off offset:2048
	global_load_dwordx4 v[8:11], v[94:95], off offset:3072
	global_load_dwordx4 v[28:31], v[20:21], off offset:1024
	s_waitcnt lgkmcnt(0)
	v_pk_add_f32 v[22:23], v[22:23], v[24:25]
	ds_bpermute_b32 v81, v138, v23
	ds_bpermute_b32 v80, v138, v22
	global_load_dwordx4 v[24:27], v[20:21], off offset:2048
	s_waitcnt lgkmcnt(0)
	v_pk_add_f32 v[80:81], v[22:23], v[80:81]
	ds_bpermute_b32 v83, v139, v81
	ds_bpermute_b32 v82, v139, v80
	global_load_dwordx4 v[20:23], v[20:21], off offset:3072
	s_waitcnt lgkmcnt(0)
	v_pk_add_f32 v[74:75], v[80:81], v[82:83]
	ds_bpermute_b32 v81, v140, v75
	ds_bpermute_b32 v80, v140, v74
	s_waitcnt lgkmcnt(0)
; DI unsigned pk2(float lo, float hi) { f32x2 v = {lo, hi}; bf16x2_t b = __builtin_convertvector(v, bf16x2_t); return __builtin_bit_cast(unsigned, b); }
; DI void phase_xnorm(const Params& p, int bid, int nb, char* lds) {
;     ...
;     for (int r = 0; r < 4; ++r)
; #pragma unroll
;       for (int i = 0; i < 4; ++i) v[r][i] = ((const f32x4*)(p.x + (size_t)(row0 + r) * 1024))[lane + 64 * i];
;     f32x4 g4[4], sh[4], sc[4];
; #pragma unroll
;     for (int i = 0; i < 4; ++i) { const int col = 4 * lane + 256 * i; g4[i] = *(const f32x4*)(p.g_pre_mix + col); sh[i] = *(const f32x4*)(mod + b * 6144 + col); sc[i] = *(const f32x4*)(mod + b * 6144 + 1024 + col); }
; #pragma unroll
;     for (int r = 0; r < 4; ++r) {
;       float ss = 0.f;
; #pragma unroll
;       for (int i = 0; i < 4; ++i) ss += v[r][i][0] * v[r][i][0] + v[r][i][1] * v[r][i][1] + v[r][i][2] * v[r][i][2] + v[r][i][3] * v[r][i][3];
;       ss = wave_sum(ss);
;       const float rstd = rsqrtf(ss * (1.f / 1024.f) + 1e-6f);
; #pragma unroll
;       for (int i = 0; i < 4; ++i) {
;         const f32x4 y = (v[r][i] * rstd * g4[i]) * (1.f + sc[i]) + sh[i];
;         u32x2 o = {pk2(y[0], y[1]), pk2(y[2], y[3])};
;         *(u32x2*)(h + (size_t)(row0 + r) * 1024 + 4 * lane + 256 * i) = o;
;         *(u32x2*)(yt + r * WP + 2 * (4 * lane + 256 * i)) = o;
;       }
	v_pk_add_f32 v[70:71], v[74:75], v[80:81]
	s_nop 0
	v_pk_fma_f32 v[154:155], v[70:71], s[26:27], v[126:127] op_sel_hi:[1,0,0]
	global_load_dwordx4 v[84:87], v[152:153], off offset:-3072
	global_load_dwordx4 v[80:83], v[152:153], off offset:-2048
	v_mul_f32_e32 v70, 0x4b800000, v155
	v_cmp_gt_f32_e32 vcc, s2, v155
	global_load_dwordx4 v[76:79], v[152:153], off offset:-1024
	global_load_dwordx4 v[72:75], v[106:107], off offset:-4096
	v_cndmask_b32_e32 v70, v155, v70, vcc
	v_rsq_f32_e32 v70, v70
	v_mul_f32_e32 v109, 0x4b800000, v154
	v_mul_f32_e32 v64, 0x45800000, v70
	v_cndmask_b32_e32 v156, v70, v64, vcc
	v_pk_mul_f32 v[62:63], v[62:63], v[156:157] op_sel_hi:[1,0]
	v_pk_mul_f32 v[60:61], v[60:61], v[156:157] op_sel_hi:[1,0]
	global_load_dwordx4 v[68:71], v[106:107], off offset:-3072
	global_load_dwordx4 v[64:67], v[106:107], off offset:-2048
	v_pk_mul_f32 v[60:61], v[0:1], v[60:61]
	v_pk_mul_f32 v[62:63], v[2:3], v[62:63]
	v_pk_fma_f32 v[60:61], v[124:125], v[60:61], v[4:5]
	v_pk_fma_f32 v[62:63], v[122:123], v[62:63], v[6:7]
	v_cvt_pk_bf16_f32 v152, v60, v61
	v_cvt_pk_bf16_f32 v153, v62, v63
	v_pk_mul_f32 v[160:161], v[58:59], v[156:157] op_sel_hi:[1,0]
	v_pk_mul_f32 v[162:163], v[56:57], v[156:157] op_sel_hi:[1,0]
	global_load_dwordx4 v[60:63], v[106:107], off offset:-1024
	global_load_dwordx4 v[56:59], v[106:107], off
	v_add_co_u32_e32 v158, vcc, s3, v134
	v_pk_mul_f32 v[34:35], v[34:35], v[156:157] op_sel_hi:[1,0]
	s_nop 0
	v_addc_co_u32_e32 v159, vcc, 0, v135, vcc
	v_add_co_u32_e32 v134, vcc, s11, v134
	v_pk_mul_f32 v[32:33], v[32:33], v[156:157] op_sel_hi:[1,0]
	s_nop 0
	v_addc_co_u32_e32 v135, vcc, 0, v135, vcc
	v_cmp_gt_f32_e32 vcc, s2, v154
	v_pk_mul_f32 v[38:39], v[38:39], v[156:157] op_sel_hi:[1,0]
	v_pk_mul_f32 v[36:37], v[36:37], v[156:157] op_sel_hi:[1,0]
	v_cndmask_b32_e32 v109, v154, v109, vcc
	v_rsq_f32_e32 v109, v109
	global_store_dwordx2 v[134:135], v[152:153], off offset:-4096
	v_mul_f32_e32 v111, 0x45800000, v109
	v_cndmask_b32_e32 v154, v109, v111, vcc
	v_add_u32_e32 v109, v90, v141
	v_pk_mul_f32 v[54:55], v[54:55], v[154:155] op_sel_hi:[1,0]
	v_pk_mul_f32 v[52:53], v[52:53], v[154:155] op_sel_hi:[1,0]
	v_pk_mul_f32 v[50:51], v[50:51], v[154:155] op_sel_hi:[1,0]
	v_pk_mul_f32 v[48:49], v[48:49], v[154:155] op_sel_hi:[1,0]
	v_pk_mul_f32 v[46:47], v[46:47], v[154:155] op_sel_hi:[1,0]
	v_pk_mul_f32 v[44:45], v[44:45], v[154:155] op_sel_hi:[1,0]
	v_pk_mul_f32 v[42:43], v[42:43], v[154:155] op_sel_hi:[1,0]
	v_pk_mul_f32 v[40:41], v[40:41], v[154:155] op_sel_hi:[1,0]
	s_waitcnt vmcnt(13)
	v_pk_mul_f32 v[36:37], v[12:13], v[36:37]
	s_waitcnt vmcnt(12)
	v_pk_mul_f32 v[32:33], v[8:9], v[32:33]
	v_pk_mul_f32 v[34:35], v[10:11], v[34:35]
	v_pk_mul_f32 v[38:39], v[14:15], v[38:39]
	ds_write_b64 v109, v[152:153] offset:33024
	v_pk_mul_f32 v[152:153], v[16:17], v[162:163]
	v_pk_mul_f32 v[154:155], v[18:19], v[160:161]
	s_waitcnt vmcnt(11)
	v_pk_fma_f32 v[152:153], v[120:121], v[152:153], v[28:29]
	s_waitcnt vmcnt(10)
	v_pk_fma_f32 v[38:39], v[116:117], v[38:39], v[26:27]
	v_pk_fma_f32 v[36:37], v[132:133], v[36:37], v[24:25]
	v_pk_fma_f32 v[154:155], v[118:119], v[154:155], v[30:31]
	v_cvt_pk_bf16_f32 v36, v36, v37
	v_cvt_pk_bf16_f32 v37, v38, v39
	global_store_dwordx2 v[158:159], v[36:37], off offset:1024
	ds_write_b64 v142, v[36:37] offset:33024
	s_waitcnt vmcnt(10)
	v_pk_fma_f32 v[34:35], v[128:129], v[34:35], v[22:23]
	v_pk_fma_f32 v[32:33], v[130:131], v[32:33], v[20:21]
	v_cvt_pk_bf16_f32 v152, v152, v153
	v_cvt_pk_bf16_f32 v32, v32, v33
	v_cvt_pk_bf16_f32 v33, v34, v35
	global_store_dwordx2 v[158:159], v[32:33], off offset:1536
	ds_write_b64 v143, v[32:33] offset:33024
	v_cvt_pk_bf16_f32 v153, v154, v155
	global_store_dwordx2 v[158:159], v[152:153], off offset:512
	ds_write_b64 v89, v[152:153] offset:33024
	s_waitcnt vmcnt(11)
	v_mov_b32_e32 v34, v85
	s_waitcnt vmcnt(10)
	v_mov_b32_e32 v35, v81
	v_mov_b32_e32 v32, v84
	v_mov_b32_e32 v33, v80
	v_pk_mul_f32 v[34:35], v[34:35], v[34:35]
	s_waitcnt vmcnt(9)
	v_mov_b32_e32 v36, v77
	v_pk_fma_f32 v[32:33], v[32:33], v[32:33], v[34:35]
	v_mov_b32_e32 v34, v86
	v_mov_b32_e32 v35, v82
	v_pk_fma_f32 v[32:33], v[34:35], v[34:35], v[32:33]
	v_mov_b32_e32 v34, v87
	v_mov_b32_e32 v35, v83
	s_waitcnt vmcnt(8)
	v_mov_b32_e32 v37, v73
	v_pk_fma_f32 v[32:33], v[34:35], v[34:35], v[32:33]
	v_mov_b32_e32 v34, v76
	v_mov_b32_e32 v35, v72
	v_pk_mul_f32 v[36:37], v[36:37], v[36:37]
	s_waitcnt vmcnt(7)
	v_mov_b32_e32 v38, v69
	v_pk_fma_f32 v[34:35], v[34:35], v[34:35], v[36:37]
	v_mov_b32_e32 v36, v78
	v_mov_b32_e32 v37, v74
	v_pk_fma_f32 v[34:35], v[36:37], v[36:37], v[34:35]
	v_mov_b32_e32 v36, v79
	v_mov_b32_e32 v37, v75
	s_waitcnt vmcnt(6)
	v_mov_b32_e32 v39, v65
	v_pk_fma_f32 v[34:35], v[36:37], v[36:37], v[34:35]
	v_mov_b32_e32 v36, v68
	v_mov_b32_e32 v37, v64
	v_pk_mul_f32 v[38:39], v[38:39], v[38:39]
	s_waitcnt vmcnt(5)
	v_mov_b32_e32 v152, v61
	v_pk_fma_f32 v[36:37], v[36:37], v[36:37], v[38:39]
	v_mov_b32_e32 v38, v70
	v_mov_b32_e32 v39, v66
	v_pk_fma_f32 v[36:37], v[38:39], v[38:39], v[36:37]
	v_mov_b32_e32 v38, v71
	v_mov_b32_e32 v39, v67
	s_waitcnt vmcnt(4)
	v_mov_b32_e32 v153, v57
	v_pk_fma_f32 v[36:37], v[38:39], v[38:39], v[36:37]
	v_mov_b32_e32 v38, v60
	v_mov_b32_e32 v39, v56
	v_pk_mul_f32 v[152:153], v[152:153], v[152:153]
	s_nop 0
	v_pk_fma_f32 v[38:39], v[38:39], v[38:39], v[152:153]
	v_mov_b32_e32 v152, v62
	v_mov_b32_e32 v153, v58
	v_pk_fma_f32 v[38:39], v[152:153], v[152:153], v[38:39]
	v_mov_b32_e32 v152, v63
	v_mov_b32_e32 v153, v59
	v_pk_fma_f32 v[38:39], v[152:153], v[152:153], v[38:39]
	v_mov_b32_e32 v152, v36
	v_mov_b32_e32 v153, v32
	v_mov_b32_e32 v32, v37
	v_pk_add_f32 v[32:33], v[152:153], v[32:33]
	v_mov_b32_e32 v36, v38
	v_mov_b32_e32 v37, v34
	v_pk_add_f32 v[32:33], v[32:33], v[36:37]
	v_mov_b32_e32 v34, v39
	v_pk_add_f32 v[32:33], v[32:33], v[34:35]
	ds_bpermute_b32 v35, v91, v33
	ds_bpermute_b32 v34, v91, v32
	v_pk_mul_f32 v[36:37], v[0:1], v[52:53]
	v_pk_mul_f32 v[38:39], v[2:3], v[54:55]
	v_pk_fma_f32 v[36:37], v[124:125], v[36:37], v[4:5]
	v_pk_fma_f32 v[38:39], v[122:123], v[38:39], v[6:7]
	s_waitcnt lgkmcnt(0)
; DI unsigned pk2(float lo, float hi) { f32x2 v = {lo, hi}; bf16x2_t b = __builtin_convertvector(v, bf16x2_t); return __builtin_bit_cast(unsigned, b); }
; DI void phase_xnorm(const Params& p, int bid, int nb, char* lds) {
;     ...
;     for (int r = 0; r < 4; ++r) {
;       float ss = 0.f;
; #pragma unroll
;       for (int i = 0; i < 4; ++i) ss += v[r][i][0] * v[r][i][0] + v[r][i][1] * v[r][i][1] + v[r][i][2] * v[r][i][2] + v[r][i][3] * v[r][i][3];
;       ss = wave_sum(ss);
;       const float rstd = rsqrtf(ss * (1.f / 1024.f) + 1e-6f);
; #pragma unroll
;       for (int i = 0; i < 4; ++i) {
;         const f32x4 y = (v[r][i] * rstd * g4[i]) * (1.f + sc[i]) + sh[i];
;         u32x2 o = {pk2(y[0], y[1]), pk2(y[2], y[3])};
;         *(u32x2*)(h + (size_t)(row0 + r) * 1024 + 4 * lane + 256 * i) = o;
;         *(u32x2*)(yt + r * WP + 2 * (4 * lane + 256 * i)) = o;
;       }
;     }
;     asm volatile("" ::: "memory");
;     f32x4 acc = {0.f, 0.f, 0.f, 0.f};
;     const char* ya = yt + (fr & 3) * WP + fq * 16; const char* wb = w16 + fr * WP + fq * 16;
; #pragma unroll
;     for (int kb = 0; kb < 4; ++kb) {
;       bf16x8 fa[8], fb[8];
; #pragma unroll
;       for (int q = 0; q < 8; ++q) { fa[q] = *(const bf16x8*)(ya + (8 * kb + q) * 64); fb[q] = *(const bf16x8*)(wb + (8 * kb + q) * 64); }
	v_pk_add_f32 v[32:33], v[32:33], v[34:35]
	ds_bpermute_b32 v35, v136, v33
	ds_bpermute_b32 v34, v136, v32
	v_cvt_pk_bf16_f32 v36, v36, v37
	v_cvt_pk_bf16_f32 v37, v38, v39
	global_store_dwordx2 v[158:159], v[36:37], off offset:2048
	ds_write_b64 v109, v[36:37] offset:35088
	s_waitcnt lgkmcnt(1)
	v_pk_add_f32 v[32:33], v[32:33], v[34:35]
	ds_bpermute_b32 v35, v137, v33
	ds_bpermute_b32 v34, v137, v32
	v_pk_mul_f32 v[36:37], v[16:17], v[48:49]
	v_pk_mul_f32 v[38:39], v[18:19], v[50:51]
	v_pk_fma_f32 v[36:37], v[120:121], v[36:37], v[28:29]
	v_pk_fma_f32 v[38:39], v[118:119], v[38:39], v[30:31]
	s_waitcnt lgkmcnt(0)
	v_pk_add_f32 v[32:33], v[32:33], v[34:35]
	ds_bpermute_b32 v35, v138, v33
	ds_bpermute_b32 v34, v138, v32
	v_cvt_pk_bf16_f32 v36, v36, v37
	v_cvt_pk_bf16_f32 v37, v38, v39
	global_store_dwordx2 v[158:159], v[36:37], off offset:2560
	ds_write_b64 v89, v[36:37] offset:35088
	s_waitcnt lgkmcnt(1)
	v_pk_add_f32 v[32:33], v[32:33], v[34:35]
	ds_bpermute_b32 v35, v139, v33
	ds_bpermute_b32 v34, v139, v32
	v_pk_mul_f32 v[36:37], v[12:13], v[44:45]
	v_pk_mul_f32 v[38:39], v[14:15], v[46:47]
	v_pk_fma_f32 v[36:37], v[132:133], v[36:37], v[24:25]
	v_pk_fma_f32 v[38:39], v[116:117], v[38:39], v[26:27]
	s_waitcnt lgkmcnt(0)
	v_pk_add_f32 v[32:33], v[32:33], v[34:35]
	ds_bpermute_b32 v35, v140, v33
	ds_bpermute_b32 v34, v140, v32
	v_cvt_pk_bf16_f32 v36, v36, v37
	v_cvt_pk_bf16_f32 v37, v38, v39
	global_store_dwordx2 v[158:159], v[36:37], off offset:3072
	ds_write_b64 v142, v[36:37] offset:35088
	s_waitcnt lgkmcnt(1)
	v_pk_add_f32 v[32:33], v[32:33], v[34:35]
	v_pk_mul_f32 v[34:35], v[8:9], v[40:41]
	v_pk_fma_f32 v[32:33], v[32:33], s[26:27], v[126:127] op_sel_hi:[1,0,0]
	v_pk_fma_f32 v[34:35], v[130:131], v[34:35], v[20:21]
	v_cmp_gt_f32_e32 vcc, s2, v33
	v_cvt_pk_bf16_f32 v34, v34, v35
	v_mul_f32_e32 v35, 0x4b800000, v33
	v_cndmask_b32_e32 v33, v33, v35, vcc
	v_rsq_f32_e32 v33, v33
	v_pk_mul_f32 v[36:37], v[10:11], v[42:43]
	s_nop 0
	v_pk_fma_f32 v[36:37], v[128:129], v[36:37], v[22:23]
	s_nop 0
	v_cvt_pk_bf16_f32 v35, v36, v37
	global_store_dwordx2 v[158:159], v[34:35], off offset:3584
	ds_write_b64 v143, v[34:35] offset:35088
	v_mul_f32_e32 v34, 0x45800000, v33
	v_cndmask_b32_e32 v34, v33, v34, vcc
	v_pk_mul_f32 v[36:37], v[86:87], v[34:35] op_sel_hi:[1,0]
	v_pk_mul_f32 v[38:39], v[84:85], v[34:35] op_sel_hi:[1,0]
	v_pk_mul_f32 v[36:37], v[2:3], v[36:37]
	v_pk_mul_f32 v[38:39], v[0:1], v[38:39]
	v_pk_fma_f32 v[36:37], v[122:123], v[36:37], v[6:7]
	v_pk_fma_f32 v[38:39], v[124:125], v[38:39], v[4:5]
	v_mul_f32_e32 v33, 0x4b800000, v32
	v_cvt_pk_bf16_f32 v38, v38, v39
	v_cvt_pk_bf16_f32 v39, v36, v37
	global_store_dwordx2 v[134:135], v[38:39], off
	ds_write_b64 v109, v[38:39] offset:37152
	v_pk_mul_f32 v[36:37], v[82:83], v[34:35] op_sel_hi:[1,0]
	v_pk_mul_f32 v[38:39], v[80:81], v[34:35] op_sel_hi:[1,0]
	v_pk_mul_f32 v[36:37], v[18:19], v[36:37]
	v_pk_mul_f32 v[38:39], v[16:17], v[38:39]
	v_pk_fma_f32 v[36:37], v[118:119], v[36:37], v[30:31]
	v_pk_fma_f32 v[38:39], v[120:121], v[38:39], v[28:29]
	v_cmp_gt_f32_e32 vcc, s2, v32
	v_cvt_pk_bf16_f32 v38, v38, v39
	v_cvt_pk_bf16_f32 v39, v36, v37
	global_store_dwordx2 v[134:135], v[38:39], off offset:512
	ds_write_b64 v89, v[38:39] offset:37152
	v_pk_mul_f32 v[36:37], v[78:79], v[34:35] op_sel_hi:[1,0]
	v_pk_mul_f32 v[38:39], v[76:77], v[34:35] op_sel_hi:[1,0]
	v_cndmask_b32_e32 v32, v32, v33, vcc
	v_pk_mul_f32 v[38:39], v[12:13], v[38:39]
	v_pk_mul_f32 v[36:37], v[14:15], v[36:37]
	v_rsq_f32_e32 v32, v32
	v_pk_fma_f32 v[36:37], v[116:117], v[36:37], v[26:27]
	v_pk_fma_f32 v[38:39], v[132:133], v[38:39], v[24:25]
	v_mul_f32_e32 v33, 0x45800000, v32
	v_cvt_pk_bf16_f32 v38, v38, v39
	v_cvt_pk_bf16_f32 v39, v36, v37
	v_pk_mul_f32 v[36:37], v[74:75], v[34:35] op_sel_hi:[1,0]
	v_pk_mul_f32 v[34:35], v[72:73], v[34:35] op_sel_hi:[1,0]
	v_pk_mul_f32 v[36:37], v[10:11], v[36:37]
	v_pk_mul_f32 v[34:35], v[8:9], v[34:35]
	v_pk_fma_f32 v[36:37], v[128:129], v[36:37], v[22:23]
	v_pk_fma_f32 v[34:35], v[130:131], v[34:35], v[20:21]
	v_cndmask_b32_e32 v32, v32, v33, vcc
	v_cvt_pk_bf16_f32 v34, v34, v35
	v_cvt_pk_bf16_f32 v35, v36, v37
	global_store_dwordx2 v[134:135], v[34:35], off offset:1536
	ds_write_b64 v143, v[34:35] offset:37152
	v_pk_mul_f32 v[34:35], v[70:71], v[32:33] op_sel_hi:[1,0]
	v_pk_mul_f32 v[36:37], v[68:69], v[32:33] op_sel_hi:[1,0]
	v_pk_mul_f32 v[2:3], v[2:3], v[34:35]
	v_pk_mul_f32 v[0:1], v[0:1], v[36:37]
	v_pk_fma_f32 v[2:3], v[122:123], v[2:3], v[6:7]
	v_pk_fma_f32 v[0:1], v[124:125], v[0:1], v[4:5]
	global_store_dwordx2 v[134:135], v[38:39], off offset:1024
	v_cvt_pk_bf16_f32 v0, v0, v1
	v_cvt_pk_bf16_f32 v1, v2, v3
	global_store_dwordx2 v[134:135], v[0:1], off offset:2048
	ds_write_b64 v109, v[0:1] offset:39216
	v_pk_mul_f32 v[0:1], v[66:67], v[32:33] op_sel_hi:[1,0]
	v_pk_mul_f32 v[2:3], v[64:65], v[32:33] op_sel_hi:[1,0]
	v_pk_mul_f32 v[0:1], v[18:19], v[0:1]
	v_pk_mul_f32 v[2:3], v[16:17], v[2:3]
	v_pk_fma_f32 v[0:1], v[118:119], v[0:1], v[30:31]
	v_pk_fma_f32 v[2:3], v[120:121], v[2:3], v[28:29]
	ds_write_b64 v142, v[38:39] offset:37152
	v_cvt_pk_bf16_f32 v2, v2, v3
	v_cvt_pk_bf16_f32 v3, v0, v1
	global_store_dwordx2 v[134:135], v[2:3], off offset:2560
	ds_write_b64 v89, v[2:3] offset:39216
	v_pk_mul_f32 v[0:1], v[62:63], v[32:33] op_sel_hi:[1,0]
	v_pk_mul_f32 v[2:3], v[60:61], v[32:33] op_sel_hi:[1,0]
	v_pk_mul_f32 v[0:1], v[14:15], v[0:1]
	v_pk_mul_f32 v[2:3], v[12:13], v[2:3]
	v_pk_fma_f32 v[0:1], v[116:117], v[0:1], v[26:27]
	v_pk_fma_f32 v[2:3], v[132:133], v[2:3], v[24:25]
	s_nop 0
	v_cvt_pk_bf16_f32 v2, v2, v3
	v_cvt_pk_bf16_f32 v3, v0, v1
	global_store_dwordx2 v[134:135], v[2:3], off offset:3072
	ds_write_b64 v142, v[2:3] offset:39216
	v_pk_mul_f32 v[0:1], v[58:59], v[32:33] op_sel_hi:[1,0]
	v_pk_mul_f32 v[2:3], v[56:57], v[32:33] op_sel_hi:[1,0]
	v_pk_mul_f32 v[0:1], v[10:11], v[0:1]
	v_pk_mul_f32 v[2:3], v[8:9], v[2:3]
	v_pk_fma_f32 v[0:1], v[128:129], v[0:1], v[22:23]
	v_pk_fma_f32 v[2:3], v[130:131], v[2:3], v[20:21]
	s_nop 0
	v_cvt_pk_bf16_f32 v2, v2, v3
	v_cvt_pk_bf16_f32 v3, v0, v1
	global_store_dwordx2 v[134:135], v[2:3], off offset:3584
	ds_write_b64 v143, v[2:3] offset:39216
	ds_read_b128 v[0:3], v144 offset:33024
	ds_read_b128 v[4:7], v144 offset:33088
	ds_read_b128 v[8:11], v145
	ds_read_b128 v[12:15], v145 offset:64
	s_waitcnt lgkmcnt(1)
; DI float sigmoidf_(float x) { return __builtin_amdgcn_rcpf(1.f + __expf(-x)); }
; DI float softplusf_(float x) { return fmaxf(x, 0.f) + log1pf(__expf(-fabsf(x))); }
; #define MFMA16(a, b, c) __builtin_amdgcn_mfma_f32_16x16x32_bf16((a), (b), (c), 0, 0, 0)
; DI void phase_xnorm(const Params& p, int bid, int nb, char* lds) {
;     ...
;     f32x4 acc = {0.f, 0.f, 0.f, 0.f};
;     const char* ya = yt + (fr & 3) * WP + fq * 16; const char* wb = w16 + fr * WP + fq * 16;
; #pragma unroll
;     for (int kb = 0; kb < 4; ++kb) {
;       bf16x8 fa[8], fb[8];
; #pragma unroll
;       for (int q = 0; q < 8; ++q) { fa[q] = *(const bf16x8*)(ya + (8 * kb + q) * 64); fb[q] = *(const bf16x8*)(wb + (8 * kb + q) * 64); }
; #pragma unroll
;       for (int q = 0; q < 8; ++q) acc = MFMA16(fa[q], fb[q], acc);
;     }
;     asm volatile("" ::: "memory");
;     if (fq == 0) {
;       const int j = fr;
; #pragma unroll
;       for (int r = 0; r < 4; ++r) { const float xx = acc[r]; float res;
;         if (j < 8) res = -softplusf_(-(xx + p.b_fgate[j]));
;         else if (j < 12) res = sigmoidf_(xx);
;         else res = -__expf(p.a_log[j - 12]) * softplusf_(xx + p.dt_bias[j - 12]);
;         small[(size_t)(row0 + r) * 16 + j] = res; }
;     }
	v_mfma_f32_16x16x32_bf16 v[0:3], v[0:3], v[8:11], 0
	ds_read_b128 v[8:11], v144 offset:33152
	ds_read_b128 v[16:19], v144 offset:33216
	s_waitcnt lgkmcnt(2)
	v_mfma_f32_16x16x32_bf16 v[0:3], v[4:7], v[12:15], v[0:3]
	ds_read_b128 v[4:7], v145 offset:128
	ds_read_b128 v[12:15], v145 offset:192
	s_waitcnt lgkmcnt(1)
	v_mfma_f32_16x16x32_bf16 v[0:3], v[8:11], v[4:7], v[0:3]
	ds_read_b128 v[4:7], v144 offset:33280
	ds_read_b128 v[8:11], v144 offset:33344
	s_waitcnt lgkmcnt(2)
	v_mfma_f32_16x16x32_bf16 v[0:3], v[16:19], v[12:15], v[0:3]
	ds_read_b128 v[12:15], v145 offset:256
	ds_read_b128 v[16:19], v145 offset:320
	s_waitcnt lgkmcnt(1)
	v_mfma_f32_16x16x32_bf16 v[0:3], v[4:7], v[12:15], v[0:3]
	ds_read_b128 v[4:7], v144 offset:33408
	ds_read_b128 v[12:15], v144 offset:33472
	s_waitcnt lgkmcnt(2)
	v_mfma_f32_16x16x32_bf16 v[0:3], v[8:11], v[16:19], v[0:3]
	ds_read_b128 v[8:11], v145 offset:384
	ds_read_b128 v[16:19], v145 offset:448
	s_waitcnt lgkmcnt(1)
	v_mfma_f32_16x16x32_bf16 v[0:3], v[4:7], v[8:11], v[0:3]
	ds_read_b128 v[4:7], v144 offset:33536
	s_waitcnt lgkmcnt(1)
	v_mfma_f32_16x16x32_bf16 v[0:3], v[12:15], v[16:19], v[0:3]
	ds_read_b128 v[8:11], v144 offset:33600
	ds_read_b128 v[12:15], v145 offset:512
	ds_read_b128 v[16:19], v145 offset:576
	s_waitcnt lgkmcnt(1)
	v_mfma_f32_16x16x32_bf16 v[0:3], v[4:7], v[12:15], v[0:3]
	ds_read_b128 v[4:7], v144 offset:33664
	ds_read_b128 v[12:15], v144 offset:33728
	s_waitcnt lgkmcnt(2)
	v_mfma_f32_16x16x32_bf16 v[0:3], v[8:11], v[16:19], v[0:3]
	ds_read_b128 v[8:11], v145 offset:640
	ds_read_b128 v[16:19], v145 offset:704
	s_waitcnt lgkmcnt(1)
	v_mfma_f32_16x16x32_bf16 v[0:3], v[4:7], v[8:11], v[0:3]
	ds_read_b128 v[4:7], v144 offset:33792
	ds_read_b128 v[8:11], v144 offset:33856
	s_waitcnt lgkmcnt(2)
	v_mfma_f32_16x16x32_bf16 v[0:3], v[12:15], v[16:19], v[0:3]
	ds_read_b128 v[12:15], v145 offset:768
	ds_read_b128 v[16:19], v145 offset:832
	s_waitcnt lgkmcnt(1)
	v_mfma_f32_16x16x32_bf16 v[0:3], v[4:7], v[12:15], v[0:3]
	ds_read_b128 v[4:7], v144 offset:33920
	ds_read_b128 v[12:15], v144 offset:33984
	s_waitcnt lgkmcnt(2)
	v_mfma_f32_16x16x32_bf16 v[0:3], v[8:11], v[16:19], v[0:3]
	ds_read_b128 v[8:11], v145 offset:896
	ds_read_b128 v[16:19], v145 offset:960
	s_waitcnt lgkmcnt(1)
	v_mfma_f32_16x16x32_bf16 v[0:3], v[4:7], v[8:11], v[0:3]
	ds_read_b128 v[4:7], v144 offset:34048
	s_waitcnt lgkmcnt(1)
	v_mfma_f32_16x16x32_bf16 v[0:3], v[12:15], v[16:19], v[0:3]
	ds_read_b128 v[8:11], v144 offset:34112
	ds_read_b128 v[12:15], v145 offset:1024
	ds_read_b128 v[16:19], v145 offset:1088
	s_waitcnt lgkmcnt(1)
	v_mfma_f32_16x16x32_bf16 v[0:3], v[4:7], v[12:15], v[0:3]
	ds_read_b128 v[4:7], v144 offset:34176
	ds_read_b128 v[12:15], v144 offset:34240
	s_waitcnt lgkmcnt(2)
	v_mfma_f32_16x16x32_bf16 v[0:3], v[8:11], v[16:19], v[0:3]
	ds_read_b128 v[8:11], v145 offset:1152
	ds_read_b128 v[16:19], v145 offset:1216
	s_waitcnt lgkmcnt(1)
	v_mfma_f32_16x16x32_bf16 v[0:3], v[4:7], v[8:11], v[0:3]
	ds_read_b128 v[4:7], v144 offset:34304
	ds_read_b128 v[8:11], v144 offset:34368
	s_waitcnt lgkmcnt(2)
	v_mfma_f32_16x16x32_bf16 v[0:3], v[12:15], v[16:19], v[0:3]
	ds_read_b128 v[12:15], v145 offset:1280
	ds_read_b128 v[16:19], v145 offset:1344
	s_waitcnt lgkmcnt(1)
	v_mfma_f32_16x16x32_bf16 v[0:3], v[4:7], v[12:15], v[0:3]
	ds_read_b128 v[4:7], v144 offset:34432
	ds_read_b128 v[12:15], v144 offset:34496
	s_waitcnt lgkmcnt(2)
	v_mfma_f32_16x16x32_bf16 v[0:3], v[8:11], v[16:19], v[0:3]
	ds_read_b128 v[8:11], v145 offset:1408
	ds_read_b128 v[16:19], v145 offset:1472
	s_waitcnt lgkmcnt(1)
	v_mfma_f32_16x16x32_bf16 v[0:3], v[4:7], v[8:11], v[0:3]
	ds_read_b128 v[4:7], v144 offset:34560
	s_waitcnt lgkmcnt(1)
	v_mfma_f32_16x16x32_bf16 v[0:3], v[12:15], v[16:19], v[0:3]
	ds_read_b128 v[8:11], v144 offset:34624
	ds_read_b128 v[12:15], v145 offset:1536
	ds_read_b128 v[16:19], v145 offset:1600
	s_waitcnt lgkmcnt(1)
	v_mfma_f32_16x16x32_bf16 v[0:3], v[4:7], v[12:15], v[0:3]
	ds_read_b128 v[4:7], v144 offset:34688
	ds_read_b128 v[12:15], v144 offset:34752
	s_waitcnt lgkmcnt(2)
	v_mfma_f32_16x16x32_bf16 v[0:3], v[8:11], v[16:19], v[0:3]
	ds_read_b128 v[8:11], v145 offset:1664
	ds_read_b128 v[16:19], v145 offset:1728
	s_waitcnt lgkmcnt(1)
	v_mfma_f32_16x16x32_bf16 v[0:3], v[4:7], v[8:11], v[0:3]
	ds_read_b128 v[4:7], v144 offset:34816
	ds_read_b128 v[8:11], v144 offset:34880
	s_waitcnt lgkmcnt(2)
	v_mfma_f32_16x16x32_bf16 v[0:3], v[12:15], v[16:19], v[0:3]
	ds_read_b128 v[12:15], v145 offset:1792
	ds_read_b128 v[16:19], v145 offset:1856
	s_waitcnt lgkmcnt(1)
	v_mfma_f32_16x16x32_bf16 v[0:3], v[4:7], v[12:15], v[0:3]
	ds_read_b128 v[4:7], v144 offset:34944
	ds_read_b128 v[12:15], v144 offset:35008
	s_waitcnt lgkmcnt(2)
	v_mfma_f32_16x16x32_bf16 v[0:3], v[8:11], v[16:19], v[0:3]
	ds_read_b128 v[8:11], v145 offset:1920
	ds_read_b128 v[16:19], v145 offset:1984
	s_waitcnt lgkmcnt(1)
	v_mfma_f32_16x16x32_bf16 v[0:3], v[4:7], v[8:11], v[0:3]
	s_waitcnt lgkmcnt(0)
	v_mfma_f32_16x16x32_bf16 v[0:3], v[12:15], v[16:19], v[0:3]
	s_nop 7
	s_nop 1
	v_bfe_u32 v243, v206, 4, 2
	v_lshlrev_b32_e32 v245, 6, v243
	v_cmp_eq_u32_e32 vcc, 1, v243
	s_nop 1
	v_cndmask_b32_e32 v0, v0, v1, vcc
	v_cmp_eq_u32_e32 vcc, 2, v243
	s_nop 1
	v_cndmask_b32_e32 v0, v0, v2, vcc
	v_cmp_eq_u32_e32 vcc, 3, v243
	s_nop 1
	v_cndmask_b32_e32 v0, v0, v3, vcc
	s_and_saveexec_b64 s[30:31], exec
	s_cbranch_execz .LBB0_93
; DI float softplusf_(float x) { return fmaxf(x, 0.f) + log1pf(__expf(-fabsf(x))); }
; DI void phase_xnorm(const Params& p, int bid, int nb, char* lds) {
;     ...
;         else res = -__expf(p.a_log[j - 12]) * softplusf_(xx + p.dt_bias[j - 12]);
	s_and_saveexec_b64 s[34:35], s[6:7]
	s_xor_b64 s[34:35], exec, s[34:35]
	s_cbranch_execz .LBB0_101
	s_and_saveexec_b64 s[38:39], s[8:9]
	s_xor_b64 s[38:39], exec, s[38:39]
	s_cbranch_execz .LBB0_98
	v_mov_b32_e32 v4, v240
	v_mov_b32_e32 v5, v241
	v_add_f32_e32 v4, v0, v4
	v_mul_f32_e64 v6, |v4|, s18
	v_exp_f32_e32 v18, v6
	v_mul_f32_e32 v5, 0x3fb8aa3b, v5
	v_exp_f32_e32 v19, v5
	v_max_f32_e32 v20, 0, v4
	v_add_f32_e32 v6, 1.0, v18
	v_add_f32_e32 v7, -1.0, v6
	v_frexp_mant_f32_e32 v8, v6
	v_cvt_f64_f32_e32 v[4:5], v6
	v_sub_f32_e32 v9, v7, v6
	v_frexp_exp_i32_f64_e32 v4, v[4:5]
	v_cmp_gt_f32_e32 vcc, s19, v8
	v_sub_f32_e32 v7, v18, v7
	v_add_f32_e32 v5, 1.0, v9
	v_subbrev_co_u32_e32 v4, vcc, 0, v4, vcc
	v_add_f32_e32 v5, v7, v5
	v_sub_u32_e32 v7, 0, v4
	v_ldexp_f32 v6, v6, v7
	v_add_f32_e32 v8, -1.0, v6
	v_add_f32_e32 v9, 1.0, v6
	v_ldexp_f32 v5, v5, v7
	v_add_f32_e32 v7, 1.0, v8
	v_add_f32_e32 v10, -1.0, v9
	v_sub_f32_e32 v7, v6, v7
	v_sub_f32_e32 v6, v6, v10
	v_add_f32_e32 v10, v5, v7
	v_add_f32_e32 v5, v5, v6
	v_add_f32_e32 v12, v9, v5
	v_rcp_f32_e32 v13, v12
	v_add_f32_e32 v7, v8, v10
	v_sub_f32_e32 v8, v7, v8
	v_sub_f32_e32 v6, v12, v9
	v_mul_f32_e32 v15, v7, v13
	v_sub_f32_e32 v14, v10, v8
	v_mul_f32_e32 v8, v12, v15
	v_sub_f32_e32 v5, v5, v6
	v_fma_f32 v10, v15, v12, -v8
	v_fmac_f32_e32 v10, v15, v5
	v_add_f32_e32 v6, v8, v10
	v_sub_f32_e32 v9, v7, v6
	v_mov_b32_e32 v11, v6
	v_pk_add_f32 v[6:7], v[6:7], v[8:9] neg_lo:[0,1] neg_hi:[0,1]
	v_cvt_f32_i32_e32 v4, v4
	v_pk_add_f32 v[6:7], v[6:7], v[10:11] neg_lo:[0,1] neg_hi:[0,1]
	v_cmp_neq_f32_e32 vcc, s29, v18
	v_add_f32_e32 v7, v14, v7
	v_add_f32_e32 v6, v6, v7
	v_add_f32_e32 v7, v9, v6
	v_mul_f32_e32 v11, v13, v7
	v_mul_f32_e32 v8, v12, v11
	v_sub_f32_e32 v9, v9, v7
	v_add_f32_e32 v16, v15, v11
	v_fma_f32 v10, v11, v12, -v8
	v_add_f32_e32 v14, v6, v9
	v_sub_f32_e32 v6, v16, v15
	v_fmac_f32_e32 v10, v11, v5
	v_sub_f32_e32 v5, v11, v6
	v_add_f32_e32 v6, v8, v10
	v_sub_f32_e32 v9, v7, v6
	v_mov_b32_e32 v11, v6
	v_pk_add_f32 v[6:7], v[6:7], v[8:9] neg_lo:[0,1] neg_hi:[0,1]
	s_nop 0
	v_pk_add_f32 v[6:7], v[6:7], v[10:11] neg_lo:[0,1] neg_hi:[0,1]
	s_nop 0
	v_add_f32_e32 v7, v14, v7
	v_add_f32_e32 v6, v6, v7
	v_add_f32_e32 v6, v9, v6
	v_mul_f32_e32 v6, v13, v6
	v_add_f32_e32 v5, v5, v6
	v_add_f32_e32 v6, v16, v5
	v_mul_f32_e32 v8, v6, v6
	v_sub_f32_e32 v9, v6, v16
	v_fmamk_f32 v10, v8, 0x3e9b6dac, v148
	v_sub_f32_e32 v9, v5, v9
	v_mul_f32_e32 v5, v6, v8
	v_fmaak_f32 v115, v8, v10, 0x3f2aaada
	v_ldexp_f32 v11, v9, 1
	v_pk_mul_f32 v[8:9], v[4:5], v[114:115]
	v_ldexp_f32 v7, v6, 1
	v_fma_f32 v6, v4, s27, -v8
	v_fmac_f32_e32 v6, 0xb102e308, v4
	v_pk_add_f32 v[4:5], v[8:9], v[6:7]
	v_mov_b32_e32 v10, v8
	v_sub_f32_e32 v14, v5, v7
	v_pk_add_f32 v[12:13], v[4:5], v[8:9] neg_lo:[0,1] neg_hi:[0,1]
	v_sub_f32_e32 v8, v9, v14
	v_add_f32_e32 v11, v11, v8
	v_pk_add_f32 v[8:9], v[4:5], v[10:11]
	v_mov_b32_e32 v7, v4
	v_mov_b32_e32 v13, v9
	v_pk_add_f32 v[16:17], v[6:7], v[12:13] neg_lo:[0,1] neg_hi:[0,1]
	v_pk_add_f32 v[6:7], v[6:7], v[12:13]
	v_mov_b32_e32 v15, v4
	v_pk_add_f32 v[12:13], v[6:7], v[4:5] op_sel:[1,0] op_sel_hi:[0,1] neg_lo:[0,1] neg_hi:[0,1]
	v_mov_b32_e32 v14, v11
	v_mov_b32_e32 v10, v9
	v_mov_b32_e32 v11, v7
	v_pk_mov_b32 v[4:5], v[4:5], v[12:13] op_sel:[1,0]
	v_pk_add_f32 v[8:9], v[8:9], v[12:13] op_sel_hi:[1,0] neg_lo:[0,1] neg_hi:[0,1]
	v_pk_add_f32 v[4:5], v[10:11], v[4:5] neg_lo:[0,1] neg_hi:[0,1]
	v_mov_b32_e32 v8, v16
	v_pk_add_f32 v[4:5], v[14:15], v[4:5] neg_lo:[0,1] neg_hi:[0,1]
	v_mov_b32_e32 v17, v7
	v_pk_add_f32 v[8:9], v[8:9], v[4:5]
	s_nop 0
	v_pk_add_f32 v[10:11], v[8:9], v[8:9] op_sel:[0,1] op_sel_hi:[1,0]
	s_nop 0
	v_pk_add_f32 v[6:7], v[6:7], v[10:11] op_sel:[1,0] op_sel_hi:[0,1]
	v_mov_b32_e32 v9, v6
	v_mov_b32_e32 v5, v10
	v_pk_add_f32 v[10:11], v[8:9], v[16:17] neg_lo:[0,1] neg_hi:[0,1]
	s_nop 0
	v_sub_f32_e32 v7, v8, v10
	v_pk_add_f32 v[4:5], v[4:5], v[10:11] neg_lo:[0,1] neg_hi:[0,1]
	v_sub_f32_e32 v7, v16, v7
	v_add_f32_e32 v4, v4, v7
	v_add_f32_e32 v4, v4, v5
	v_add_f32_e32 v4, v6, v4
	v_cndmask_b32_e32 v4, v149, v4, vcc
	v_cmp_ngt_f32_e32 vcc, -1.0, v18
	s_nop 1
	v_cndmask_b32_e32 v4, v150, v4, vcc
	v_cmp_neq_f32_e32 vcc, -1.0, v18
	s_nop 1
	v_cndmask_b32_e32 v4, v151, v4, vcc
	v_cmp_lt_f32_e64 vcc, |v18|, s40
	s_nop 1
	v_cndmask_b32_e32 v4, v4, v18, vcc
	v_add_f32_e32 v4, v20, v4
	v_mul_f32_e64 v6, v4, -v19

; DI void phase_xnorm(const Params& p, int bid, int nb, char* lds) {
;     ...
;         small[(size_t)(row0 + r) * 16 + j] = res; }
.LBB0_103:
	s_or_b64 exec, exec, s[34:35]
	v_lshl_add_u64 v[4:5], s[84:85], 0, v[102:103]
	v_add_co_u32_e32 v8, vcc, 0x1700000, v4
	s_nop 1
	v_addc_co_u32_e32 v9, vcc, 0, v5, vcc
	v_add_co_u32_e32 v8, vcc, v245, v8
	s_nop 1
	v_addc_co_u32_e32 v9, vcc, 0, v9, vcc
	global_store_dword v[8:9], v6, off
	s_branch .LBB0_93
	s_and_saveexec_b64 s[34:35], s[6:7]
	s_xor_b64 s[34:35], exec, s[34:35]
	s_cbranch_execz .LBB0_109
	s_and_saveexec_b64 s[38:39], s[8:9]
	s_xor_b64 s[38:39], exec, s[38:39]
	s_cbranch_execz .LBB0_106
	v_mov_b32_e32 v0, v240
	v_mov_b32_e32 v6, v241
	v_add_f32_e32 v0, v1, v0
	v_mul_f32_e64 v7, |v0|, s18
	v_exp_f32_e32 v20, v7
	v_mul_f32_e32 v6, 0x3fb8aa3b, v6
	v_exp_f32_e32 v21, v6
	v_max_f32_e32 v0, 0, v0
	v_add_f32_e32 v8, 1.0, v20
	v_add_f32_e32 v9, -1.0, v8
	v_frexp_mant_f32_e32 v10, v8
	v_cvt_f64_f32_e32 v[6:7], v8
	v_sub_f32_e32 v11, v9, v8
	v_frexp_exp_i32_f64_e32 v6, v[6:7]
	v_cmp_gt_f32_e32 vcc, s19, v10
	v_sub_f32_e32 v9, v20, v9
	v_add_f32_e32 v7, 1.0, v11
	v_subbrev_co_u32_e32 v6, vcc, 0, v6, vcc
	v_add_f32_e32 v7, v9, v7
	v_sub_u32_e32 v9, 0, v6
	v_ldexp_f32 v8, v8, v9
	v_add_f32_e32 v10, -1.0, v8
	v_add_f32_e32 v11, 1.0, v8
	v_ldexp_f32 v7, v7, v9
	v_add_f32_e32 v9, 1.0, v10
	v_add_f32_e32 v12, -1.0, v11
	v_sub_f32_e32 v9, v8, v9
	v_sub_f32_e32 v8, v8, v12
	v_add_f32_e32 v12, v7, v9
	v_add_f32_e32 v7, v7, v8
	v_add_f32_e32 v14, v11, v7
	v_rcp_f32_e32 v15, v14
	v_add_f32_e32 v9, v10, v12
	v_sub_f32_e32 v10, v9, v10
	v_sub_f32_e32 v8, v14, v11
	v_mul_f32_e32 v17, v9, v15
	v_sub_f32_e32 v16, v12, v10
	v_mul_f32_e32 v10, v14, v17
	v_sub_f32_e32 v7, v7, v8
	v_fma_f32 v12, v17, v14, -v10
	v_fmac_f32_e32 v12, v17, v7
	v_add_f32_e32 v8, v10, v12
	v_sub_f32_e32 v11, v9, v8
	v_mov_b32_e32 v13, v8
	v_pk_add_f32 v[8:9], v[8:9], v[10:11] neg_lo:[0,1] neg_hi:[0,1]
	v_cvt_f32_i32_e32 v6, v6
	v_pk_add_f32 v[8:9], v[8:9], v[12:13] neg_lo:[0,1] neg_hi:[0,1]
	v_cmp_neq_f32_e32 vcc, s29, v20
	v_add_f32_e32 v9, v16, v9
	v_add_f32_e32 v8, v8, v9
	v_add_f32_e32 v9, v11, v8
	v_mul_f32_e32 v13, v15, v9
	v_mul_f32_e32 v10, v14, v13
	v_sub_f32_e32 v11, v11, v9
	v_add_f32_e32 v18, v17, v13
	v_fma_f32 v12, v13, v14, -v10
	v_add_f32_e32 v16, v8, v11
	v_sub_f32_e32 v8, v18, v17
	v_fmac_f32_e32 v12, v13, v7
	v_sub_f32_e32 v7, v13, v8
	v_add_f32_e32 v8, v10, v12
	v_sub_f32_e32 v11, v9, v8
	v_mov_b32_e32 v13, v8
	v_pk_add_f32 v[8:9], v[8:9], v[10:11] neg_lo:[0,1] neg_hi:[0,1]
	s_nop 0
	v_pk_add_f32 v[8:9], v[8:9], v[12:13] neg_lo:[0,1] neg_hi:[0,1]
	s_nop 0
	v_add_f32_e32 v9, v16, v9
	v_add_f32_e32 v8, v8, v9
	v_add_f32_e32 v8, v11, v8
	v_mul_f32_e32 v8, v15, v8
	v_add_f32_e32 v7, v7, v8
	v_add_f32_e32 v8, v18, v7
	v_mul_f32_e32 v10, v8, v8
	v_sub_f32_e32 v11, v8, v18
	v_fmamk_f32 v12, v10, 0x3e9b6dac, v148
	v_sub_f32_e32 v11, v7, v11
	v_mul_f32_e32 v7, v8, v10
	v_fmaak_f32 v115, v10, v12, 0x3f2aaada
	v_ldexp_f32 v13, v11, 1
	v_pk_mul_f32 v[10:11], v[6:7], v[114:115]
	v_ldexp_f32 v9, v8, 1
	v_fma_f32 v8, v6, s27, -v10
	v_fmac_f32_e32 v8, 0xb102e308, v6
	v_pk_add_f32 v[6:7], v[10:11], v[8:9]
	v_mov_b32_e32 v12, v10
	v_sub_f32_e32 v16, v7, v9
	v_pk_add_f32 v[14:15], v[6:7], v[10:11] neg_lo:[0,1] neg_hi:[0,1]
	v_sub_f32_e32 v10, v11, v16
	v_add_f32_e32 v13, v13, v10
	v_pk_add_f32 v[10:11], v[6:7], v[12:13]
	v_mov_b32_e32 v9, v6
	v_mov_b32_e32 v15, v11
	v_pk_add_f32 v[18:19], v[8:9], v[14:15] neg_lo:[0,1] neg_hi:[0,1]
	v_pk_add_f32 v[8:9], v[8:9], v[14:15]
	v_mov_b32_e32 v17, v6
	v_pk_add_f32 v[14:15], v[8:9], v[6:7] op_sel:[1,0] op_sel_hi:[0,1] neg_lo:[0,1] neg_hi:[0,1]
	v_mov_b32_e32 v16, v13
	v_mov_b32_e32 v12, v11
	v_mov_b32_e32 v13, v9
	v_pk_mov_b32 v[6:7], v[6:7], v[14:15] op_sel:[1,0]
	v_pk_add_f32 v[10:11], v[10:11], v[14:15] op_sel_hi:[1,0] neg_lo:[0,1] neg_hi:[0,1]
	v_pk_add_f32 v[6:7], v[12:13], v[6:7] neg_lo:[0,1] neg_hi:[0,1]
	v_mov_b32_e32 v10, v18
	v_pk_add_f32 v[6:7], v[16:17], v[6:7] neg_lo:[0,1] neg_hi:[0,1]
	v_mov_b32_e32 v19, v9
	v_pk_add_f32 v[10:11], v[10:11], v[6:7]
	s_nop 0
	v_pk_add_f32 v[12:13], v[10:11], v[10:11] op_sel:[0,1] op_sel_hi:[1,0]
	s_nop 0
	v_pk_add_f32 v[8:9], v[8:9], v[12:13] op_sel:[1,0] op_sel_hi:[0,1]
	v_mov_b32_e32 v11, v8
	v_mov_b32_e32 v7, v12
	v_pk_add_f32 v[12:13], v[10:11], v[18:19] neg_lo:[0,1] neg_hi:[0,1]
	s_nop 0
	v_sub_f32_e32 v9, v10, v12
	v_pk_add_f32 v[6:7], v[6:7], v[12:13] neg_lo:[0,1] neg_hi:[0,1]
	v_sub_f32_e32 v9, v18, v9
	v_add_f32_e32 v6, v6, v9
	v_add_f32_e32 v6, v6, v7
	v_add_f32_e32 v6, v8, v6
	v_cndmask_b32_e32 v6, v149, v6, vcc
	v_cmp_ngt_f32_e32 vcc, -1.0, v20
	s_nop 1
	v_cndmask_b32_e32 v6, v150, v6, vcc
	v_cmp_neq_f32_e32 vcc, -1.0, v20
	s_nop 1
	v_cndmask_b32_e32 v6, v151, v6, vcc
	v_cmp_lt_f32_e64 vcc, |v20|, s40
	s_nop 1
	v_cndmask_b32_e32 v6, v6, v20, vcc
	v_add_f32_e32 v0, v0, v6
	v_mul_f32_e64 v0, v0, -v21
